# router phase: static s_setprio 1 for the four converter waves (router waves at 0); on top of v6
# baseline (speedup 1.0000x reference)
.LBB0_1223:
	s_andn2_b64 vcc, exec, s[0:1]
	s_cbranch_vccnz .LBB0_1245
	s_setprio 1
	s_add_i32 s8, s33, -4
	s_lshl_b32 s0, s2, 2
	s_add_i32 s20, s8, s0
	s_cmpk_gt_i32 s20, 0x5fff
	s_cbranch_scc1 .LBB0_1245
	s_add_i32 s0, s20, 0xc000
	s_cmpk_lt_i32 s20, 0x4000
	s_cselect_b32 s9, s20, s0
	s_cmp_gt_i32 s9, 0xffff
	s_cbranch_scc0 .LBB0_1227
	s_load_dwordx2 s[0:1], s[16:17], 0x110
	s_add_i32 s4, s9, 0xffff0000
	s_mov_b32 s7, 0
	s_lshr_b32 s6, s4, 10
	s_lshl_b64 s[4:5], s[6:7], 24
	s_waitcnt lgkmcnt(0)
	s_add_u32 s0, s0, s4
	s_addc_u32 s1, s1, s5
	s_lshl_b32 s4, s9, 1
	s_and_b32 s10, s4, 0x780
	s_lshl_b32 s4, s10, 13
	s_add_u32 s0, s0, s4
	s_addc_u32 s1, s1, 0
	s_lshl_b32 s4, s9, 5
	s_and_b32 s11, s4, 0x7e0
	s_lshl_b32 s4, s11, 2
	s_add_u32 s4, s0, s4
	s_addc_u32 s5, s1, 0
	s_lshl_b64 s[0:1], s[6:7], 22
	s_lshl_b32 s6, s11, 11
	s_add_u32 s0, s18, s0
	s_addc_u32 s1, s19, s1
	s_add_u32 s0, s0, s6
	s_addc_u32 s1, s1, 0
	s_add_u32 s0, s0, s10
	s_addc_u32 s1, s1, 0
	s_add_u32 s0, s0, 0x24e00000
	s_addc_u32 s1, s1, 0
	s_mov_b32 s21, 0x42800000
	s_cbranch_execz .LBB0_1228
	s_branch .LBB0_1229
